# W2 tiles 9088..12287 converted inside the GEMM1 SwiGLU epilogue (register path, loads hidden under epilogue VALU); P7 tail queue empty; P1 converts W1 only
# speedup vs baseline: 1.0128x; 1.0128x over previous
.LBB0_86:
	s_cmp_lt_i32 s50, 2
	s_cselect_b64 s[6:7], -1, 0
	s_and_b64 s[0:1], s[6:7], s[2:3]
	s_andn2_b64 vcc, exec, s[0:1]
	v_writelane_b32 v254, s60, 4
	s_cbranch_vccnz .LBB0_260
	s_mov_b64 s[2:3], s[80:81]
	s_load_dwordx2 s[8:9], s[2:3], 0xa8
	s_cmpk_lg_i32 s56, 0x100
	s_cselect_b32 s0, s56, 0xb4
	s_cmp_ge_i32 s78, s0
	s_mov_b64 s[4:5], -1
	s_cbranch_scc0 .LBB0_145
	s_sub_i32 s1, s78, s0
	s_cmpk_gt_i32 s1, 0x1fff
	s_cbranch_scc1 .LBB0_144
	s_sub_i32 s20, s56, s0
	s_abs_i32 s4, s20
	v_cvt_f32_u32_e32 v1, s4
	s_load_dwordx2 s[10:11], s[2:3], 0x78
	s_load_dwordx2 s[12:13], s[2:3], 0x88
	s_sub_i32 s2, s20, s1
	s_add_i32 s3, s2, 0x1fff
	v_rcp_iflag_f32_e32 v1, v1
	s_sub_i32 s2, 0xffffe001, s2
	s_xor_b32 s14, s3, s20
	s_sub_i32 s5, 0, s4
	v_mul_f32_e32 v1, 0x4f7ffffe, v1
	v_cvt_u32_f32_e32 v1, v1
	s_max_i32 s2, s3, s2
	s_ashr_i32 s3, s14, 31
	v_readfirstlane_b32 s14, v1
	s_mul_i32 s5, s5, s14
	s_mul_hi_u32 s5, s14, s5
	s_add_i32 s14, s14, s5
	s_mul_hi_u32 s5, s2, s14
	s_mul_i32 s14, s5, s4
	s_sub_i32 s2, s2, s14
	s_add_i32 s14, s5, 1
	s_sub_i32 s15, s2, s4
	s_cmp_ge_u32 s2, s4
	s_cselect_b32 s5, s14, s5
	s_cselect_b32 s2, s15, s2
	s_add_i32 s14, s5, 1
	s_cmp_ge_u32 s2, s4
	s_cselect_b32 s2, s14, s5
	s_xor_b32 s2, s2, s3
	s_sub_i32 s29, s2, s3
	s_lshl_b32 s21, s29, 2
	s_add_i32 s22, s21, -1
	s_cmp_gt_i32 s29, 0
	s_cselect_b64 s[2:3], -1, 0
	s_and_b64 s[4:5], s[2:3], exec
	s_cselect_b32 s18, 0, s22
	s_ashr_i32 s4, s18, 2
	s_mul_i32 s17, s4, s20
	s_add_i32 s17, s17, s1
	s_cmpk_gt_i32 s17, 0x1fff
	s_mov_b32 s5, 0
	s_cbranch_scc0 .LBB0_91
	s_add_i32 s4, s17, 0xffffe000
	s_lshr_b32 s4, s4, 7
	s_lshl_b64 s[4:5], s[4:5], 24
	s_waitcnt lgkmcnt(0)
	s_add_u32 s14, s12, s4
	s_addc_u32 s15, s13, s5
	s_lshl_b32 s4, s17, 4
	s_and_b32 s26, s4, 0x780
	s_lshl_b32 s4, s17, 8
	s_and_b32 s16, s4, 0x700
	s_mov_b64 s[4:5], 0x800
	s_cbranch_execz .LBB0_92
	s_branch .LBB0_93

.LBB0_367:
	s_lshr_b32 s0, s56, 31
	s_add_i32 s0, s56, s0
	s_ashr_i32 s0, s0, 1
	v_readlane_b32 s78, v254, 5
	s_cmp_ge_i32 s78, s0
	v_readlane_b32 s79, v254, 8
	v_readlane_b32 s60, v254, 4
	s_cbranch_scc0 .LBB0_409
	s_sub_i32 s10, s78, s0
	s_cmpk_gt_u32 s10, 0x37f
	s_waitcnt vmcnt(0) lgkmcnt(0)
	s_barrier
	s_cbranch_scc1 .LBB0_409
	s_sub_i32 s0, s56, s0
	s_abs_i32 s2, s0
	v_cvt_f32_u32_e32 v2, s2
	s_sub_i32 s3, s0, s10
	s_add_i32 s4, s3, 0x37f
	s_sub_i32 s3, 0xfffffc81, s3
	v_rcp_iflag_f32_e32 v2, v2
	s_xor_b32 s6, s4, s0
	s_sub_i32 s5, 0, s2
	s_max_i32 s3, s4, s3
	v_mul_f32_e32 v2, 0x4f7ffffe, v2
	v_cvt_u32_f32_e32 v2, v2
	s_ashr_i32 s4, s6, 31
	s_add_i32 s1, s10, 0x2000
	v_readfirstlane_b32 s6, v2
	s_mul_i32 s5, s5, s6
	s_mul_hi_u32 s5, s6, s5
	s_add_i32 s6, s6, s5
	s_mul_hi_u32 s5, s3, s6
	s_mul_i32 s6, s5, s2
	s_sub_i32 s3, s3, s6
	s_add_i32 s7, s5, 1
	s_sub_i32 s6, s3, s2
	s_cmp_ge_u32 s3, s2
	s_cselect_b32 s5, s7, s5
	s_cselect_b32 s3, s6, s3
	s_add_i32 s6, s5, 1
	s_cmp_ge_u32 s3, s2
	s_cselect_b32 s2, s6, s5
	s_xor_b32 s2, s2, s4
	s_sub_i32 s18, s2, s4
	s_lshl_b32 s12, s18, 2
	s_add_i32 s13, s12, -1
	s_cmp_gt_i32 s18, 0
	s_cselect_b64 s[2:3], -1, 0
	s_and_b64 s[4:5], s[2:3], exec
	s_cselect_b32 s11, 0, s13
	s_ashr_i32 s4, s11, 2
	s_mul_i32 s9, s4, s0
	s_add_i32 s9, s9, s1
	s_cmpk_gt_i32 s9, 0x1fff
	s_mov_b32 s5, 0
	s_cbranch_scc0 .LBB0_371
	s_add_i32 s4, s9, 0xffffe000
	s_lshr_b32 s4, s4, 7
	s_lshl_b64 s[4:5], s[4:5], 24
	v_readlane_b32 s34, v254, 13
	v_readlane_b32 s35, v254, 14
	s_add_u32 s6, s34, s4
	s_addc_u32 s7, s35, s5
	s_lshl_b32 s4, s9, 4
	s_and_b32 s19, s4, 0x780
	s_lshl_b32 s4, s9, 8
	v_readlane_b32 s30, v254, 11
	s_and_b32 s8, s4, 0x700
	v_readlane_b32 s31, v254, 12
	s_mov_b64 s[4:5], 0x800
	s_cbranch_execz .LBB0_372
	s_branch .LBB0_373

.LBB0_387:
	s_max_i32 s9, s12, 1
	s_add_u32 s18, s66, 0x5ee00000
	s_addc_u32 s19, s67, 0
	s_ashr_i32 s7, s6, 31
	s_lshl_b64 s[6:7], s[6:7], 2
	s_add_u32 s4, s4, s6
	v_add_u32_e32 v3, s8, v14
	v_mov_b32_e32 v11, 0
	s_addc_u32 s5, s5, s7
	v_mad_i64_i32 v[12:13], s[6:7], s2, v3, 0
	v_lshl_add_u64 v[12:13], v[12:13], 2, s[4:5]
	v_mov_b32_e32 v3, v11
	v_lshl_add_u64 v[12:13], v[12:13], 0, v[2:3]
	s_mov_b64 s[6:7], 0x300
	s_add_i32 s27, 0, 0x18000
	v_lshl_add_u64 v[12:13], v[12:13], 0, s[6:7]
	s_add_i32 m0, s27, s14
	v_add_u32_e32 v3, s8, v15
	global_load_lds_dwordx4 v[12:13], off nt
	v_mad_i64_i32 v[12:13], s[28:29], s2, v3, 0
	v_lshl_add_u64 v[12:13], v[12:13], 2, s[4:5]
	v_mov_b32_e32 v5, v11
	v_lshl_add_u64 v[12:13], v[12:13], 0, v[4:5]
	v_lshl_add_u64 v[12:13], v[12:13], 0, s[6:7]
	s_add_i32 m0, s27, s15
	v_add_u32_e32 v3, s8, v16
	global_load_lds_dwordx4 v[12:13], off nt
	v_mad_i64_i32 v[12:13], s[28:29], s2, v3, 0
	v_lshl_add_u64 v[12:13], v[12:13], 2, s[4:5]
	v_mov_b32_e32 v7, v11
	v_lshl_add_u64 v[12:13], v[12:13], 0, v[6:7]
	v_lshl_add_u64 v[12:13], v[12:13], 0, s[6:7]
	s_add_i32 m0, s27, s16
	v_add_u32_e32 v3, s8, v1
	global_load_lds_dwordx4 v[12:13], off nt
	v_mad_i64_i32 v[12:13], s[2:3], s2, v3, 0
	v_lshl_add_u64 v[12:13], v[12:13], 2, s[4:5]
	v_mov_b32_e32 v9, v11
	v_lshl_add_u64 v[12:13], v[12:13], 0, v[8:9]
	v_lshl_add_u64 v[12:13], v[12:13], 0, s[6:7]
	s_add_i32 m0, s27, s17
	v_lshrrev_b32_e32 v19, 3, v162
	global_load_lds_dwordx4 v[12:13], off nt
	v_readlane_b32 s2, v254, 15
	v_and_b32_e32 v3, 7, v0
	v_lshrrev_b32_e32 v9, 1, v162
	v_or_b32_e32 v17, s2, v19
	v_lshrrev_b32_e32 v7, 2, v17
	v_bitop3_b32 v7, v7, v0, 7 bitop3:0x78
	v_lshl_add_u32 v5, v3, 12, 0
	v_lshlrev_b32_e32 v7, 4, v7
	v_and_b32_e32 v9, 12, v9
	v_add3_u32 v18, v5, v7, v9
	ds_read2st64_b32 v[12:13], v18 offset1:1
	ds_read2st64_b32 v[20:21], v18 offset0:2 offset1:3
	ds_read2st64_b32 v[22:23], v18 offset0:4 offset1:5
	ds_read2st64_b32 v[24:25], v18 offset0:6 offset1:7
	v_lshlrev_b32_e32 v10, 4, v3
	s_lshl_b32 s2, s10, 15
	s_waitcnt lgkmcnt(0)
	v_mul_f32_e32 v7, 0x42000000, v20
	v_mul_f32_e32 v3, 0x42000000, v12
	v_mul_f32_e32 v5, 0x42000000, v13
	ds_read2st64_b32 v[12:13], v18 offset0:8 offset1:9
	v_mul_f32_e32 v9, 0x42000000, v21
	v_mul_f32_e32 v26, 0x42000000, v22
	v_mul_f32_e32 v27, 0x42000000, v23
	v_mul_f32_e32 v28, 0x42000000, v24
	v_mul_f32_e32 v29, 0x42000000, v25
	ds_read2st64_b32 v[20:21], v18 offset0:10 offset1:11
	ds_read2st64_b32 v[22:23], v18 offset0:12 offset1:13
	ds_read2st64_b32 v[24:25], v18 offset0:14 offset1:15
	s_add_i32 s2, s2, 0x0
	s_and_b32 s2, s2, 0x7c00000
	s_waitcnt lgkmcnt(0)
	v_mul_f32_e32 v30, 0x42000000, v12
	v_mul_f32_e32 v13, 0x42000000, v13
	v_mul_f32_e32 v31, 0x42000000, v20
	v_mul_f32_e32 v32, 0x42000000, v21
	v_mul_f32_e32 v33, 0x42000000, v22
	v_mul_f32_e32 v34, 0x42000000, v23
	v_mov_b32_e32 v20, v11
	v_mov_b32_e32 v21, v11
	v_mov_b32_e32 v22, v11
	v_mov_b32_e32 v23, v11
	s_add_u32 s4, s18, s2
	v_cvt_pk_fp8_f32 v20, v3, v5
	v_cvt_pk_fp8_f32 v21, v26, v27
	v_cvt_pk_fp8_f32 v22, v30, v13
	v_cvt_pk_fp8_f32 v23, v33, v34
	s_addc_u32 s5, s19, 0
	s_lshl_b32 s6, s1, 8
	s_and_b32 s6, s6, 0x700
	v_mul_f32_e32 v3, 0x42000000, v24
	v_mul_f32_e32 v5, 0x42000000, v25
	v_add_u32_e32 v12, s6, v17
	v_mov_b32_e32 v13, v11
	s_lshl_b32 s2, s1, 4
	v_cvt_pk_fp8_f32 v20, v7, v9 op_sel:[0,0,1]
	v_cvt_pk_fp8_f32 v21, v28, v29 op_sel:[0,0,1]
	v_cvt_pk_fp8_f32 v22, v31, v32 op_sel:[0,0,1]
	v_cvt_pk_fp8_f32 v23, v3, v5 op_sel:[0,0,1]
	v_lshlrev_b64 v[24:25], 11, v[12:13]
	s_mov_b32 s3, 0
	s_and_b32 s2, s2, 0x780
	v_lshl_add_u64 v[24:25], s[4:5], 0, v[24:25]
	v_lshl_add_u64 v[24:25], v[24:25], 0, s[2:3]
	v_lshl_add_u64 v[24:25], v[24:25], 0, v[10:11]
	s_cmp_eq_u32 s9, 1
	global_store_dwordx4 v[24:25], v[20:23], off nt
	s_cbranch_scc1 .LBB0_408
	s_min_i32 s27, s13, 4
	s_ashr_i32 s6, s27, 2
	s_waitcnt vmcnt(9)
	s_barrier
	s_mul_i32 s29, s6, s0
	s_add_i32 s29, s29, s1
	s_cmpk_lt_i32 s29, 0x2000
	s_cbranch_scc1 .LBB0_390
	s_add_i32 s6, s29, 0xffffe000
	s_lshr_b32 s6, s6, 7
	s_mov_b32 s7, 0
	s_lshl_b64 s[6:7], s[6:7], 24
	s_add_u32 s8, s34, s6
	s_addc_u32 s9, s35, s7
	s_lshl_b32 s6, s29, 4
	s_and_b32 s28, s6, 0x780
	s_lshl_b32 s6, s29, 8
	s_and_b32 s10, s6, 0x700
	s_mov_b64 s[6:7], 0
	s_branch .LBB0_391

.LBB0_712:
	s_or_b64 exec, exec, s[20:21]
	s_add_u32 s0, s16, 0x4ee00000
	s_addc_u32 s1, s17, 0
	v_readfirstlane_b32 s2, v0
	s_cmp_ge_i32 s47, s33
	v_lshlrev_b32_e32 v1, 2, v0
	s_waitcnt lgkmcnt(0)
	s_barrier
	s_cbranch_scc1 .LBB0_734
	v_lshlrev_b32_e32 v2, 4, v0
	v_and_b32_e32 v3, 32, v0
	v_bitop3_b32 v2, v2, v3, 48 bitop3:0x6c
	v_bfe_u32 v3, v0, 3, 25
	v_bfe_u32 v4, v0, 2, 4
	v_and_or_b32 v163, v0, 64, v2
	v_lshrrev_b32_e32 v2, 3, v0
	v_or_b32_e32 v3, 64, v3
	s_movk_i32 s5, 0x70
	v_and_or_b32 v188, v2, 48, v4
	v_and_or_b32 v189, v3, s5, v4
	v_lshrrev_b32_e32 v4, 5, v0
	v_lshrrev_b32_e32 v7, 1, v0
	v_and_b32_e32 v4, 4, v4
	v_bfe_u32 v5, v0, 2, 2
	v_and_b32_e32 v7, 24, v7
	v_or3_b32 v4, v4, v5, v7
	v_and_or_b32 v2, v2, 32, v4
	v_lshl_or_b32 v166, v2, 11, v163
	v_mul_f32_e32 v2, 0x4f7ffffe, v6
	v_cvt_u32_f32_e32 v2, v2
	s_lshr_b32 s4, s2, 6
	s_lshr_b32 s3, s2, 8
	s_lshl_b32 s5, s4, 10
	v_readfirstlane_b32 s58, v2
	s_mul_i32 s34, s34, s58
	s_add_u32 s18, s16, 0x2600000
	s_mul_hi_u32 s22, s58, s34
	s_addc_u32 s19, s17, 0
	s_abs_i32 s21, s47
	s_add_i32 s58, s58, s22
	s_mul_hi_u32 s22, s21, s58
	s_movk_i32 s20, 0x60
	s_mul_i32 s23, s22, s53
	v_and_or_b32 v3, v3, s20, v4
	s_ashr_i32 s20, s47, 31
	s_ashr_i32 s55, s46, 31
	s_sub_i32 s21, s21, s23
	s_xor_b32 s20, s20, s55
	s_add_i32 s23, s22, 1
	s_sub_i32 s24, s21, s53
	s_cmp_ge_u32 s21, s53
	s_cselect_b32 s22, s23, s22
	s_cselect_b32 s21, s24, s21
	s_add_i32 s23, s22, 1
	s_cmp_ge_u32 s21, s53
	s_cselect_b32 s21, s23, s22
	s_xor_b32 s21, s21, s20
	s_sub_i32 s20, s21, s20
	s_mul_i32 s21, s20, s46
	s_sub_i32 s21, s47, s21
	s_ashr_i32 s22, s21, 31
	s_lshr_b32 s22, s22, 30
	s_add_i32 s22, s21, s22
	s_mov_b32 s86, s79
	s_ashr_i32 s79, s22, 2
	s_and_b32 s22, s22, -4
	s_lshl_b32 s20, s20, 2
	s_sub_i32 s21, s21, s22
	s_add_i32 s38, s21, s20
	s_add_i32 s20, s79, 0
	s_add_i32 s20, s20, 0x27d40
	v_lshl_or_b32 v164, v3, 11, v163
	v_mov_b32_e32 v2, s20
	s_add_i32 s20, 0, 0x20400
	v_lshlrev_b32_e32 v3, 1, v188
	v_lshlrev_b32_e32 v5, 1, v189
	v_add_u32_e32 v4, s20, v3
	v_add_u32_e32 v7, s20, v5
	s_add_i32 s20, 0, 0x20500
	v_add_u32_e32 v3, s20, v3
	v_add_u32_e32 v5, s20, v5
	ds_read_u8 v6, v2
	ds_read_u16 v2, v4
	ds_read_u16 v4, v7
	ds_read_u16 v3, v3
	ds_read_u16 v5, v5
	s_waitcnt lgkmcnt(4)
	v_readfirstlane_b32 s20, v6
	s_and_b32 s20, s20, 0xff
	s_ashr_i32 s39, s38, 31
	s_lshl_b32 s22, s20, 23
	s_lshl_b64 s[20:21], s[38:39], 19
	s_add_u32 s22, s0, s22
	s_addc_u32 s23, s1, 0
	s_add_u32 s40, s22, s20
	s_addc_u32 s41, s23, s21
	s_add_i32 s59, s5, 0
	s_add_i32 s60, s59, 0x10000
	s_add_i32 s61, s59, 0x12000
	s_mov_b32 m0, s60
	s_add_u32 s20, s40, 0x40000
	global_load_lds_dwordx4 v166, s[40:41]
	s_mov_b32 m0, s61
	s_addc_u32 s21, s41, 0
	s_add_i32 s62, s59, 0x14000
	global_load_lds_dwordx4 v164, s[40:41]
	s_mov_b32 m0, s62
	s_add_i32 s63, s59, 0x16000
	global_load_lds_dwordx4 v166, s[20:21]
	s_mov_b32 m0, s63
	s_waitcnt lgkmcnt(0)
	v_lshl_or_b32 v168, v2, 11, v163
	global_load_lds_dwordx4 v164, s[20:21]
	s_mov_b32 m0, s59
	s_add_i32 s64, s59, 0x2000
	v_lshl_or_b32 v170, v4, 11, v163
	global_load_lds_dwordx4 v168, s[18:19]
	s_mov_b32 m0, s64
	s_add_i32 s65, s59, 0x4000
	v_lshl_or_b32 v172, v3, 11, v163
	global_load_lds_dwordx4 v170, s[18:19]
	s_mov_b32 m0, s65
	s_add_i32 s66, s59, 0x6000
	v_lshl_or_b32 v174, v5, 11, v163
	global_load_lds_dwordx4 v172, s[18:19]
	s_mov_b32 m0, s66
	v_mov_b32_e32 v169, 0
	global_load_lds_dwordx4 v174, s[18:19]
	v_mov_b32_e32 v167, v169
	v_mov_b32_e32 v165, v169
	s_cmp_eq_u32 s3, 1
	s_mov_b64 s[84:85], s[80:81]
	s_mov_b32 s80, 0
	v_and_b32_e32 v249, 7, v162
	v_lshrrev_b32_e32 v250, 3, v162
	v_lshlrev_b32_e32 v248, 5, v249
	v_lshl_add_u32 v248, v250, 2, v248
	v_lshlrev_b32_e32 v251, 4, v249
	v_lshl_add_u32 v249, v250, 17, v251
	v_lshl_add_u32 v250, v250, 13, v251
	v_mov_b32_e32 v252, 0x42000000
	v_mov_b32_e32 v253, 0x42000000
	v_lshl_add_u64 v[4:5], s[40:41], 0, v[166:167]
	v_lshl_add_u64 v[2:3], s[40:41], 0, v[164:165]
	s_cselect_b64 s[20:21], -1, 0
	s_cmp_lg_u32 s3, 1
	v_mov_b32_e32 v171, v169
	s_cbranch_scc1 .LBB0_715
	s_barrier

.LBB0_730:
	v_readlane_b32 s92, v254, 5
	s_nop 3
	s_lshl_b32 s93, s80, 8
	s_add_u32 s92, s92, s93
	s_add_u32 s92, s92, 896
	s_cmp_lt_u32 s92, 0x1000
	s_cselect_b32 s32, 1, 0
	s_cbranch_scc0 .Lp7c_skip1
	s_lshr_b32 s93, s92, 3
	s_lshl_b32 s93, s93, 20
	s_and_b32 s94, s92, 7
	s_lshl_b32 s95, s94, 10
	s_or_b32 s93, s93, s95
	s_lshl_b32 s95, s57, 7
	s_or_b32 s93, s93, s95
	s_add_u32 s90, s14, s93
	s_addc_u32 s91, s15, 0
	s_lshr_b32 s93, s92, 7
	s_lshl_b32 s93, s93, 22
	s_lshl_b32 s94, s94, 19
	s_or_b32 s93, s93, s94
	s_bfe_u32 s94, s92, 0x40003
	s_lshl_b32 s94, s94, 7
	s_or_b32 s93, s93, s94
	s_lshl_b32 s94, s57, 16
	s_or_b32 s93, s93, s94
	s_add_u32 s93, s93, 0x5ee00000
	s_add_u32 s88, s48, s93
	s_addc_u32 s89, s49, 0
	global_load_dwordx4 v[216:219], v249, s[90:91] nt
	s_add_u32 s90, s90, 0x2000
	s_addc_u32 s91, s91, 0
	global_load_dwordx4 v[220:223], v249, s[90:91] nt
	s_add_u32 s90, s90, 0x2000
	s_addc_u32 s91, s91, 0
	global_load_dwordx4 v[224:227], v249, s[90:91] nt
	s_add_u32 s90, s90, 0x2000
	s_addc_u32 s91, s91, 0
	global_load_dwordx4 v[228:231], v249, s[90:91] nt
	s_add_u32 s90, s90, 0x2000
	s_addc_u32 s91, s91, 0
	global_load_dwordx4 v[232:235], v249, s[90:91] nt
	s_add_u32 s90, s90, 0x2000
	s_addc_u32 s91, s91, 0
	global_load_dwordx4 v[236:239], v249, s[90:91] nt
	s_add_u32 s90, s90, 0x2000
	s_addc_u32 s91, s91, 0
	global_load_dwordx4 v[240:243], v249, s[90:91] nt
	s_add_u32 s90, s90, 0x2000
	s_addc_u32 s91, s91, 0
	global_load_dwordx4 v[244:247], v249, s[90:91] nt
	s_add_u32 s90, s90, 0x2000
	s_addc_u32 s91, s91, 0
.Lp7c_skip1:
	s_lshl_b32 s31, s80, 11
	s_and_b32 s31, s31, 0x800
	v_add_u32_e32 v2, s31, v191
	s_nop 15
	s_nop 3
	ds_read_b128 v[14:17], v2
	ds_read_b128 v[10:13], v2 offset:16
	v_lshl_add_u32 v22, s79, 8, v171
	v_ashrrev_i32_e32 v23, 31, v22
	v_lshl_or_b32 v20, s38, 7, v190
	s_waitcnt lgkmcnt(0)
	v_fmamk_f32 v3, v158, 0x3d000000, v14
	v_min_f32_e32 v18, 0x40e00000, v3
	v_mul_f32_e32 v3, 0xc01d265f, v18
	v_exp_f32_e32 v19, v3
	v_fmamk_f32 v26, v160, 0x3d000000, v10
	v_add_f32_e32 v24, 1.0, v15
	v_min_f32_e32 v26, 0x40e00000, v26
	v_add_f32_e32 v19, 1.0, v19
	v_rcp_f32_e32 v19, v19
	v_fmamk_f32 v15, v154, 0x3d000000, v24
	v_mul_f32_e32 v27, 0xc01d265f, v26
	v_med3_f32 v15, v15, s73, v210
	v_mul_f32_e32 v18, v18, v19
	v_fmamk_f32 v19, v159, 0x3d000000, v16
	v_min_f32_e32 v19, 0x40e00000, v19
	v_mul_f32_e32 v25, 0xc01d265f, v19
	v_exp_f32_e32 v25, v25
	v_exp_f32_e32 v27, v27
	v_mul_f32_e32 v18, v15, v18
	v_add_f32_e32 v15, 1.0, v17
	v_add_f32_e32 v25, 1.0, v25
	v_rcp_f32_e32 v25, v25
	v_fmamk_f32 v17, v155, 0x3d000000, v15
	v_med3_f32 v17, v17, s73, v210
	ds_read_b128 v[6:9], v2 offset:32
	ds_read_b128 v[2:5], v2 offset:48
	v_mul_f32_e32 v19, v19, v25
	v_mul_f32_e32 v19, v17, v19
	v_add_f32_e32 v17, 1.0, v27
	v_rcp_f32_e32 v25, v17
	s_waitcnt lgkmcnt(0)
	v_fmamk_f32 v28, v150, 0x3d000000, v6
	v_min_f32_e32 v28, 0x40e00000, v28
	v_add_f32_e32 v17, 1.0, v11
	v_mul_f32_e32 v25, v26, v25
	v_fmamk_f32 v26, v161, 0x3d000000, v12
	v_min_f32_e32 v26, 0x40e00000, v26
	v_mul_f32_e32 v27, 0xc01d265f, v26
	v_exp_f32_e32 v27, v27
	v_mul_f32_e32 v29, 0xc01d265f, v28
	v_fmamk_f32 v11, v156, 0x3d000000, v17
	v_exp_f32_e32 v29, v29
	v_add_f32_e32 v27, 1.0, v27
	v_rcp_f32_e32 v27, v27
	v_med3_f32 v11, v11, s73, v210
	v_add_f32_e32 v13, 1.0, v13
	v_mul_f32_e32 v25, v11, v25
	v_fmamk_f32 v11, v157, 0x3d000000, v13
	v_med3_f32 v11, v11, s73, v210
	v_mul_f32_e32 v26, v26, v27
	v_mul_f32_e32 v30, v11, v26
	v_add_f32_e32 v11, 1.0, v29
	v_rcp_f32_e32 v26, v11
	v_fmamk_f32 v27, v151, 0x3d000000, v8
	v_min_f32_e32 v27, 0x40e00000, v27
	v_add_f32_e32 v11, 1.0, v7
	v_mul_f32_e32 v26, v28, v26
	v_mul_f32_e32 v28, 0xc01d265f, v27
	v_exp_f32_e32 v28, v28
	v_fmamk_f32 v7, v146, 0x3d000000, v11
	v_med3_f32 v7, v7, s73, v210
	v_mul_f32_e32 v29, v7, v26
	v_add_f32_e32 v26, 1.0, v28
	v_fmamk_f32 v28, v152, 0x3d000000, v2
	v_min_f32_e32 v28, 0x40e00000, v28
	v_rcp_f32_e32 v26, v26
	v_mul_f32_e32 v31, 0xc01d265f, v28
	v_exp_f32_e32 v31, v31
	v_add_f32_e32 v7, 1.0, v9
	v_fmamk_f32 v9, v147, 0x3d000000, v7
	v_med3_f32 v9, v9, s73, v210
	v_mul_f32_e32 v26, v27, v26
	v_mul_f32_e32 v32, v9, v26
	v_add_f32_e32 v9, 1.0, v31
	v_rcp_f32_e32 v26, v9
	v_add_f32_e32 v9, 1.0, v3
	v_fmamk_f32 v3, v148, 0x3d000000, v9
	v_med3_f32 v3, v3, s73, v210
	v_mul_f32_e32 v26, v28, v26
	v_mul_f32_e32 v28, v3, v26
	v_fmamk_f32 v3, v153, 0x3d000000, v4
	v_min_f32_e32 v31, 0x40e00000, v3
	v_mul_f32_e32 v3, 0xc01d265f, v31
	v_exp_f32_e32 v26, v3
	v_mov_b32_e32 v27, v169
	v_add_f32_e32 v3, 1.0, v5
	v_cvt_pk_fp8_f32 v27, v29, v32
	v_add_f32_e32 v26, 1.0, v26
	v_rcp_f32_e32 v33, v26
	v_fmamk_f32 v5, v149, 0x3d000000, v3
	v_mov_b32_e32 v26, v169
	v_med3_f32 v5, v5, s73, v210
	v_cvt_pk_fp8_f32 v26, v18, v19
	v_mul_f32_e32 v18, v31, v33
	v_mul_f32_e32 v5, v5, v18
	v_cvt_pk_fp8_f32 v27, v28, v5 op_sel:[0,0,1]
	v_fmamk_f32 v5, v142, 0x3d000000, v14
	v_min_f32_e32 v5, 0x40e00000, v5
	v_lshlrev_b64 v[18:19], 11, v[22:23]
	v_mul_f32_e32 v23, 0xc01d265f, v5
	v_exp_f32_e32 v23, v23
	v_fmamk_f32 v28, v143, 0x3d000000, v16
	v_min_f32_e32 v28, 0x40e00000, v28
	v_mul_f32_e32 v29, 0xc01d265f, v28
	v_add_f32_e32 v23, 1.0, v23
	v_rcp_f32_e32 v23, v23
	v_cvt_pk_fp8_f32 v26, v25, v30 op_sel:[0,0,1]
	v_fmamk_f32 v25, v138, 0x3d000000, v24
	v_exp_f32_e32 v29, v29
	v_med3_f32 v25, v25, s73, v210
	v_mul_f32_e32 v5, v5, v23
	v_mul_f32_e32 v5, v25, v5
	v_fmamk_f32 v25, v144, 0x3d000000, v10
	v_min_f32_e32 v25, 0x40e00000, v25
	v_add_f32_e32 v23, 1.0, v29
	v_mul_f32_e32 v29, 0xc01d265f, v25
	v_rcp_f32_e32 v23, v23
	v_exp_f32_e32 v29, v29
	v_fmamk_f32 v30, v139, 0x3d000000, v15
	v_med3_f32 v30, v30, s73, v210
	v_mul_f32_e32 v23, v28, v23
	v_add_f32_e32 v28, 1.0, v29
	v_rcp_f32_e32 v28, v28
	v_mul_f32_e32 v23, v30, v23
	v_fmamk_f32 v31, v134, 0x3d000000, v6
	v_min_f32_e32 v31, 0x40e00000, v31
	v_mul_f32_e32 v25, v25, v28
	v_fmamk_f32 v28, v145, 0x3d000000, v12
	v_min_f32_e32 v28, 0x40e00000, v28
	v_mul_f32_e32 v30, 0xc01d265f, v28
	v_exp_f32_e32 v30, v30
	v_mul_f32_e32 v32, 0xc01d265f, v31
	v_fmamk_f32 v29, v140, 0x3d000000, v17
	v_exp_f32_e32 v32, v32
	v_add_f32_e32 v30, 1.0, v30
	v_rcp_f32_e32 v30, v30
	v_med3_f32 v29, v29, s73, v210
	v_mul_f32_e32 v25, v29, v25
	v_fmamk_f32 v29, v141, 0x3d000000, v13
	v_med3_f32 v29, v29, s73, v210
	v_mul_f32_e32 v28, v28, v30
	v_mul_f32_e32 v30, v29, v28
	v_add_f32_e32 v29, 1.0, v32
	v_rcp_f32_e32 v29, v29
	v_fmamk_f32 v32, v135, 0x3d000000, v8
	v_min_f32_e32 v32, 0x40e00000, v32
	v_mul_f32_e32 v33, 0xc01d265f, v32
	v_fmamk_f32 v28, v130, 0x3d000000, v11
	v_exp_f32_e32 v33, v33
	v_med3_f32 v28, v28, s73, v210
	v_mul_f32_e32 v29, v31, v29
	v_mul_f32_e32 v31, v28, v29
	v_fmamk_f32 v29, v136, 0x3d000000, v2
	v_min_f32_e32 v29, 0x40e00000, v29
	v_add_f32_e32 v28, 1.0, v33
	v_mul_f32_e32 v33, 0xc01d265f, v29
	v_rcp_f32_e32 v28, v28
	v_exp_f32_e32 v33, v33
	v_fmamk_f32 v130, v131, 0x3d000000, v7
	v_med3_f32 v130, v130, s73, v210
	v_mul_f32_e32 v28, v32, v28
	v_add_f32_e32 v32, 1.0, v33
	v_rcp_f32_e32 v32, v32
	v_mul_f32_e32 v33, v130, v28
	v_fmamk_f32 v28, v132, 0x3d000000, v9
	v_med3_f32 v28, v28, s73, v210
	v_mul_f32_e32 v29, v29, v32
	v_fmamk_f32 v32, v137, 0x3d000000, v4
	v_min_f32_e32 v32, 0x40e00000, v32
	v_mul_f32_e32 v130, 0xc01d265f, v32
	v_exp_f32_e32 v130, v130
	v_mul_f32_e32 v131, v28, v29
	v_fmamk_f32 v28, v133, 0x3d000000, v3
	v_med3_f32 v132, v28, s73, v210
	v_add_f32_e32 v28, 1.0, v130
	v_rcp_f32_e32 v130, v28
	v_mov_b32_e32 v29, v169
	v_cvt_pk_fp8_f32 v29, v31, v33
	v_mov_b32_e32 v28, v169
	v_cvt_pk_fp8_f32 v28, v5, v23
	v_mul_f32_e32 v5, v32, v130
	v_mul_f32_e32 v5, v132, v5
	v_cvt_pk_fp8_f32 v29, v131, v5 op_sel:[0,0,1]
	s_cmp_eq_u32 s32, 0
	s_cbranch_scc1 .Lp7c_skip2
	global_load_dwordx4 v[130:133], v249, s[90:91] nt
	s_add_u32 s90, s90, 0x2000
	s_addc_u32 s91, s91, 0
	global_load_dwordx4 v[134:137], v249, s[90:91] nt
	s_add_u32 s90, s90, 0x2000
	s_addc_u32 s91, s91, 0
	global_load_dwordx4 v[138:141], v249, s[90:91] nt
	s_add_u32 s90, s90, 0x2000
	s_addc_u32 s91, s91, 0
	global_load_dwordx4 v[142:145], v249, s[90:91] nt
	s_add_u32 s90, s90, 0x2000
	s_addc_u32 s91, s91, 0
	global_load_dwordx4 v[146:149], v249, s[90:91] nt
	s_add_u32 s90, s90, 0x2000
	s_addc_u32 s91, s91, 0
	global_load_dwordx4 v[150:153], v249, s[90:91] nt
	s_add_u32 s90, s90, 0x2000
	s_addc_u32 s91, s91, 0
	global_load_dwordx4 v[154:157], v249, s[90:91] nt
	s_add_u32 s90, s90, 0x2000
	s_addc_u32 s91, s91, 0
	global_load_dwordx4 v[158:161], v249, s[90:91] nt
.Lp7c_skip2:
	v_fmamk_f32 v5, v126, 0x3d000000, v14
	v_ashrrev_i32_e32 v21, 31, v20
	v_lshl_add_u64 v[18:19], s[22:23], 0, v[18:19]
	v_min_f32_e32 v5, 0x40e00000, v5
	v_lshl_add_u64 v[18:19], v[18:19], 0, v[20:21]
	v_mul_f32_e32 v23, 0xc01d265f, v5
	global_store_dwordx2 v[18:19], v[26:27], off
	v_or_b32_e32 v26, 16, v22
	v_exp_f32_e32 v23, v23
	v_ashrrev_i32_e32 v27, 31, v26
	v_cvt_pk_fp8_f32 v28, v25, v30 op_sel:[0,0,1]
	v_lshlrev_b64 v[26:27], 11, v[26:27]
	v_lshl_add_u64 v[26:27], s[22:23], 0, v[26:27]
	v_lshl_add_u64 v[26:27], v[26:27], 0, v[20:21]
	v_add_f32_e32 v23, 1.0, v23
	global_store_dwordx2 v[26:27], v[28:29], off
	v_rcp_f32_e32 v23, v23
	v_fmamk_f32 v28, v127, 0x3d000000, v16
	v_min_f32_e32 v28, 0x40e00000, v28
	v_mul_f32_e32 v29, 0xc01d265f, v28
	v_fmamk_f32 v25, v122, 0x3d000000, v24
	v_exp_f32_e32 v29, v29
	v_med3_f32 v25, v25, s73, v210
	v_mul_f32_e32 v5, v5, v23
	v_mul_f32_e32 v5, v25, v5
	v_fmamk_f32 v25, v128, 0x3d000000, v10
	v_min_f32_e32 v25, 0x40e00000, v25
	v_add_f32_e32 v23, 1.0, v29
	v_mul_f32_e32 v29, 0xc01d265f, v25
	v_rcp_f32_e32 v23, v23
	v_exp_f32_e32 v29, v29
	v_fmamk_f32 v30, v123, 0x3d000000, v15
	v_med3_f32 v30, v30, s73, v210
	v_mul_f32_e32 v23, v28, v23
	v_add_f32_e32 v28, 1.0, v29
	v_rcp_f32_e32 v28, v28
	v_mul_f32_e32 v23, v30, v23
	v_fmamk_f32 v31, v118, 0x3d000000, v6
	v_min_f32_e32 v31, 0x40e00000, v31
	v_mul_f32_e32 v25, v25, v28
	v_fmamk_f32 v28, v129, 0x3d000000, v12
	v_min_f32_e32 v28, 0x40e00000, v28
	v_mul_f32_e32 v30, 0xc01d265f, v28
	v_exp_f32_e32 v30, v30
	v_mul_f32_e32 v32, 0xc01d265f, v31
	v_fmamk_f32 v29, v124, 0x3d000000, v17
	v_exp_f32_e32 v32, v32
	v_add_f32_e32 v30, 1.0, v30
	v_rcp_f32_e32 v30, v30
	v_med3_f32 v29, v29, s73, v210
	v_mul_f32_e32 v25, v29, v25
	v_fmamk_f32 v29, v125, 0x3d000000, v13
	v_med3_f32 v29, v29, s73, v210
	v_mul_f32_e32 v28, v28, v30
	v_mul_f32_e32 v30, v29, v28
	v_add_f32_e32 v29, 1.0, v32
	v_rcp_f32_e32 v29, v29
	v_fmamk_f32 v32, v119, 0x3d000000, v8
	v_min_f32_e32 v32, 0x40e00000, v32
	v_mul_f32_e32 v33, 0xc01d265f, v32
	v_fmamk_f32 v28, v114, 0x3d000000, v11
	v_exp_f32_e32 v33, v33
	v_med3_f32 v28, v28, s73, v210
	v_mul_f32_e32 v29, v31, v29
	v_mul_f32_e32 v31, v28, v29
	v_fmamk_f32 v29, v120, 0x3d000000, v2
	v_min_f32_e32 v29, 0x40e00000, v29
	v_add_f32_e32 v28, 1.0, v33
	v_mul_f32_e32 v33, 0xc01d265f, v29
	v_rcp_f32_e32 v28, v28
	v_exp_f32_e32 v33, v33
	v_fmamk_f32 v114, v115, 0x3d000000, v7
	v_med3_f32 v114, v114, s73, v210
	v_mul_f32_e32 v28, v32, v28
	v_add_f32_e32 v32, 1.0, v33
	v_rcp_f32_e32 v32, v32
	v_mul_f32_e32 v33, v114, v28
	v_fmamk_f32 v28, v116, 0x3d000000, v9
	v_med3_f32 v28, v28, s73, v210
	v_mul_f32_e32 v29, v29, v32
	v_fmamk_f32 v32, v121, 0x3d000000, v4
	v_min_f32_e32 v32, 0x40e00000, v32
	v_mul_f32_e32 v114, 0xc01d265f, v32
	v_exp_f32_e32 v114, v114
	v_mul_f32_e32 v115, v28, v29
	v_fmamk_f32 v28, v117, 0x3d000000, v3
	v_med3_f32 v116, v28, s73, v210
	v_add_f32_e32 v28, 1.0, v114
	v_rcp_f32_e32 v114, v28
	v_mov_b32_e32 v29, v169
	v_cvt_pk_fp8_f32 v29, v31, v33
	v_mov_b32_e32 v28, v169
	v_cvt_pk_fp8_f32 v28, v5, v23
	v_mul_f32_e32 v5, v32, v114
	v_mul_f32_e32 v5, v116, v5
	v_cvt_pk_fp8_f32 v29, v115, v5 op_sel:[0,0,1]
	v_fmamk_f32 v5, v110, 0x3d000000, v14
	v_min_f32_e32 v5, 0x40e00000, v5
	v_cvt_pk_fp8_f32 v28, v25, v30 op_sel:[0,0,1]
	v_mul_f32_e32 v25, 0xc01d265f, v5
	v_or_b32_e32 v26, 32, v22
	v_exp_f32_e32 v25, v25
	v_ashrrev_i32_e32 v27, 31, v26
	v_lshlrev_b64 v[26:27], 11, v[26:27]
	v_lshl_add_u64 v[26:27], s[22:23], 0, v[26:27]
	v_lshl_add_u64 v[26:27], v[26:27], 0, v[20:21]
	v_add_f32_e32 v25, 1.0, v25
	global_store_dwordx2 v[26:27], v[28:29], off
	v_rcp_f32_e32 v25, v25
	v_fmamk_f32 v27, v111, 0x3d000000, v16
	v_min_f32_e32 v27, 0x40e00000, v27
	v_mul_f32_e32 v28, 0xc01d265f, v27
	v_fmamk_f32 v26, v106, 0x3d000000, v24
	v_exp_f32_e32 v28, v28
	v_med3_f32 v26, v26, s73, v210
	v_mul_f32_e32 v5, v5, v25
	v_mul_f32_e32 v5, v26, v5
	v_fmamk_f32 v26, v112, 0x3d000000, v10
	v_min_f32_e32 v26, 0x40e00000, v26
	v_add_f32_e32 v25, 1.0, v28
	v_mul_f32_e32 v28, 0xc01d265f, v26
	v_rcp_f32_e32 v25, v25
	v_exp_f32_e32 v28, v28
	v_fmamk_f32 v29, v107, 0x3d000000, v15
	v_med3_f32 v29, v29, s73, v210
	v_mul_f32_e32 v25, v27, v25
	v_add_f32_e32 v27, 1.0, v28
	v_rcp_f32_e32 v27, v27
	v_mul_f32_e32 v25, v29, v25
	v_fmamk_f32 v30, v102, 0x3d000000, v6
	v_min_f32_e32 v30, 0x40e00000, v30
	v_mul_f32_e32 v26, v26, v27
	v_fmamk_f32 v27, v113, 0x3d000000, v12
	v_min_f32_e32 v27, 0x40e00000, v27
	v_mul_f32_e32 v29, 0xc01d265f, v27
	v_exp_f32_e32 v29, v29
	v_mul_f32_e32 v31, 0xc01d265f, v30
	v_fmamk_f32 v28, v108, 0x3d000000, v17
	v_exp_f32_e32 v31, v31
	v_add_f32_e32 v29, 1.0, v29
	v_rcp_f32_e32 v29, v29
	v_med3_f32 v28, v28, s73, v210
	v_mul_f32_e32 v28, v28, v26
	v_fmamk_f32 v26, v109, 0x3d000000, v13
	v_med3_f32 v26, v26, s73, v210
	v_mul_f32_e32 v27, v27, v29
	v_mul_f32_e32 v29, v26, v27
	v_add_f32_e32 v27, 1.0, v31
	v_rcp_f32_e32 v27, v27
	v_fmamk_f32 v31, v103, 0x3d000000, v8
	v_min_f32_e32 v31, 0x40e00000, v31
	v_mul_f32_e32 v32, 0xc01d265f, v31
	v_fmamk_f32 v26, v98, 0x3d000000, v11
	v_exp_f32_e32 v32, v32
	v_med3_f32 v26, v26, s73, v210
	v_mul_f32_e32 v27, v30, v27
	v_mul_f32_e32 v30, v26, v27
	v_fmamk_f32 v27, v104, 0x3d000000, v2
	v_min_f32_e32 v27, 0x40e00000, v27
	v_add_f32_e32 v26, 1.0, v32
	v_mul_f32_e32 v32, 0xc01d265f, v27
	v_rcp_f32_e32 v26, v26
	v_exp_f32_e32 v32, v32
	v_fmamk_f32 v33, v99, 0x3d000000, v7
	v_med3_f32 v33, v33, s73, v210
	v_mul_f32_e32 v26, v31, v26
	v_add_f32_e32 v31, 1.0, v32
	v_rcp_f32_e32 v31, v31
	v_mul_f32_e32 v32, v33, v26
	v_fmamk_f32 v26, v100, 0x3d000000, v9
	v_med3_f32 v26, v26, s73, v210
	v_mul_f32_e32 v27, v27, v31
	v_fmamk_f32 v31, v105, 0x3d000000, v4
	v_min_f32_e32 v31, 0x40e00000, v31
	v_mul_f32_e32 v33, 0xc01d265f, v31
	v_exp_f32_e32 v33, v33
	v_mul_f32_e32 v98, v26, v27
	v_fmamk_f32 v26, v101, 0x3d000000, v3
	v_med3_f32 v99, v26, s73, v210
	v_add_f32_e32 v26, 1.0, v33
	v_rcp_f32_e32 v33, v26
	v_mov_b32_e32 v27, v169
	v_cvt_pk_fp8_f32 v27, v30, v32
	v_mov_b32_e32 v26, v169
	v_cvt_pk_fp8_f32 v26, v5, v25
	v_mul_f32_e32 v5, v31, v33
	v_mul_f32_e32 v5, v99, v5
	v_cvt_pk_fp8_f32 v27, v98, v5 op_sel:[0,0,1]
	v_fmamk_f32 v5, v94, 0x3d000000, v14
	v_min_f32_e32 v5, 0x40e00000, v5
	v_or_b32_e32 v22, 48, v22
	v_mul_f32_e32 v25, 0xc01d265f, v5
	v_ashrrev_i32_e32 v23, 31, v22
	v_cvt_pk_fp8_f32 v26, v28, v29 op_sel:[0,0,1]
	v_exp_f32_e32 v25, v25
	v_lshlrev_b64 v[22:23], 11, v[22:23]
	v_lshl_add_u64 v[22:23], s[22:23], 0, v[22:23]
	v_lshl_add_u64 v[20:21], v[22:23], 0, v[20:21]
	global_store_dwordx2 v[20:21], v[26:27], off
	v_add_f32_e32 v21, 1.0, v25
	v_fmamk_f32 v22, v95, 0x3d000000, v16
	v_rcp_f32_e32 v21, v21
	v_min_f32_e32 v22, 0x40e00000, v22
	v_mul_f32_e32 v23, 0xc01d265f, v22
	v_exp_f32_e32 v23, v23
	v_fmamk_f32 v20, v90, 0x3d000000, v24
	v_mul_f32_e32 v5, v5, v21
	v_fmamk_f32 v21, v96, 0x3d000000, v10
	v_med3_f32 v20, v20, s73, v210
	v_min_f32_e32 v21, 0x40e00000, v21
	v_mul_f32_e32 v5, v20, v5
	v_add_f32_e32 v20, 1.0, v23
	v_mul_f32_e32 v23, 0xc01d265f, v21
	v_rcp_f32_e32 v20, v20
	v_exp_f32_e32 v23, v23
	v_fmamk_f32 v25, v91, 0x3d000000, v15
	v_med3_f32 v25, v25, s73, v210
	v_mul_f32_e32 v20, v22, v20
	v_add_f32_e32 v22, 1.0, v23
	v_rcp_f32_e32 v22, v22
	v_mul_f32_e32 v23, v25, v20
	v_fmamk_f32 v20, v92, 0x3d000000, v17
	v_med3_f32 v20, v20, s73, v210
	v_mul_f32_e32 v21, v21, v22
	v_fmamk_f32 v22, v97, 0x3d000000, v12
	v_min_f32_e32 v22, 0x40e00000, v22
	v_mul_f32_e32 v25, 0xc01d265f, v22
	v_exp_f32_e32 v25, v25
	v_mul_f32_e32 v26, v20, v21
	v_fmamk_f32 v20, v93, 0x3d000000, v13
	v_med3_f32 v20, v20, s73, v210
	v_add_f32_e32 v21, 1.0, v25
	v_fmamk_f32 v25, v86, 0x3d000000, v6
	v_min_f32_e32 v25, 0x40e00000, v25
	v_rcp_f32_e32 v21, v21
	v_mul_f32_e32 v27, 0xc01d265f, v25
	v_exp_f32_e32 v27, v27
	v_fmamk_f32 v29, v83, 0x3d000000, v7
	v_mul_f32_e32 v21, v22, v21
	v_mul_f32_e32 v22, v20, v21
	v_add_f32_e32 v21, 1.0, v27
	v_rcp_f32_e32 v21, v21
	v_fmamk_f32 v27, v87, 0x3d000000, v8
	v_min_f32_e32 v27, 0x40e00000, v27
	v_mul_f32_e32 v28, 0xc01d265f, v27
	v_fmamk_f32 v20, v82, 0x3d000000, v11
	v_exp_f32_e32 v28, v28
	v_med3_f32 v20, v20, s73, v210
	v_mul_f32_e32 v21, v25, v21
	v_mul_f32_e32 v25, v20, v21
	v_fmamk_f32 v21, v88, 0x3d000000, v2
	v_min_f32_e32 v21, 0x40e00000, v21
	v_add_f32_e32 v20, 1.0, v28
	v_mul_f32_e32 v28, 0xc01d265f, v21
	v_rcp_f32_e32 v20, v20
	v_exp_f32_e32 v28, v28
	v_med3_f32 v29, v29, s73, v210
	v_mul_f32_e32 v20, v27, v20
	v_add_f32_e32 v27, 1.0, v28
	v_rcp_f32_e32 v27, v27
	v_mul_f32_e32 v28, v29, v20
	v_fmamk_f32 v20, v84, 0x3d000000, v9
	v_med3_f32 v20, v20, s73, v210
	v_mul_f32_e32 v21, v21, v27
	v_fmamk_f32 v27, v89, 0x3d000000, v4
	v_min_f32_e32 v27, 0x40e00000, v27
	v_mul_f32_e32 v29, 0xc01d265f, v27
	v_exp_f32_e32 v29, v29
	v_mul_f32_e32 v30, v20, v21
	v_fmamk_f32 v20, v85, 0x3d000000, v3
	v_med3_f32 v31, v20, s73, v210
	v_add_f32_e32 v20, 1.0, v29
	v_rcp_f32_e32 v29, v20
	v_mov_b32_e32 v21, v169
	v_cvt_pk_fp8_f32 v21, v25, v28
	v_mov_b32_e32 v20, v169
	v_cvt_pk_fp8_f32 v20, v5, v23
	v_mul_f32_e32 v5, v27, v29
	v_mul_f32_e32 v5, v31, v5
	v_cvt_pk_fp8_f32 v21, v30, v5 op_sel:[0,0,1]
	v_fmamk_f32 v5, v78, 0x3d000000, v14
	v_min_f32_e32 v5, 0x40e00000, v5
	v_cvt_pk_fp8_f32 v20, v26, v22 op_sel:[0,0,1]
	v_mul_f32_e32 v22, 0xc01d265f, v5
	v_exp_f32_e32 v25, v22
	v_add_co_u32_e32 v22, vcc, s74, v18
	v_fmamk_f32 v29, v67, 0x3d000000, v7
	s_nop 0
	v_addc_co_u32_e32 v23, vcc, 0, v19, vcc
	global_store_dwordx2 v[22:23], v[20:21], off
	v_add_f32_e32 v21, 1.0, v25
	v_fmamk_f32 v22, v79, 0x3d000000, v16
	v_rcp_f32_e32 v21, v21
	v_min_f32_e32 v22, 0x40e00000, v22
	v_mul_f32_e32 v23, 0xc01d265f, v22
	v_exp_f32_e32 v23, v23
	v_fmamk_f32 v20, v74, 0x3d000000, v24
	v_mul_f32_e32 v5, v5, v21
	v_fmamk_f32 v21, v80, 0x3d000000, v10
	v_med3_f32 v20, v20, s73, v210
	v_min_f32_e32 v21, 0x40e00000, v21
	v_mul_f32_e32 v5, v20, v5
	v_add_f32_e32 v20, 1.0, v23
	v_mul_f32_e32 v23, 0xc01d265f, v21
	v_rcp_f32_e32 v20, v20
	v_exp_f32_e32 v23, v23
	v_fmamk_f32 v25, v75, 0x3d000000, v15
	v_med3_f32 v25, v25, s73, v210
	v_mul_f32_e32 v20, v22, v20
	v_add_f32_e32 v22, 1.0, v23
	v_rcp_f32_e32 v22, v22
	v_mul_f32_e32 v23, v25, v20
	v_fmamk_f32 v20, v76, 0x3d000000, v17
	v_med3_f32 v20, v20, s73, v210
	v_mul_f32_e32 v21, v21, v22
	v_fmamk_f32 v22, v81, 0x3d000000, v12
	v_min_f32_e32 v22, 0x40e00000, v22
	v_mul_f32_e32 v25, 0xc01d265f, v22
	v_exp_f32_e32 v25, v25
	v_mul_f32_e32 v26, v20, v21
	v_fmamk_f32 v20, v77, 0x3d000000, v13
	v_med3_f32 v20, v20, s73, v210
	v_add_f32_e32 v21, 1.0, v25
	v_fmamk_f32 v25, v70, 0x3d000000, v6
	v_min_f32_e32 v25, 0x40e00000, v25
	v_rcp_f32_e32 v21, v21
	v_mul_f32_e32 v27, 0xc01d265f, v25
	v_exp_f32_e32 v27, v27
	v_med3_f32 v29, v29, s73, v210
	v_mul_f32_e32 v21, v22, v21
	v_mul_f32_e32 v22, v20, v21
	v_add_f32_e32 v21, 1.0, v27
	v_rcp_f32_e32 v21, v21
	v_fmamk_f32 v27, v71, 0x3d000000, v8
	v_min_f32_e32 v27, 0x40e00000, v27
	v_mul_f32_e32 v28, 0xc01d265f, v27
	v_fmamk_f32 v20, v66, 0x3d000000, v11
	v_exp_f32_e32 v28, v28
	v_med3_f32 v20, v20, s73, v210
	v_mul_f32_e32 v21, v25, v21
	v_mul_f32_e32 v25, v20, v21
	v_fmamk_f32 v21, v72, 0x3d000000, v2
	v_min_f32_e32 v21, 0x40e00000, v21
	v_add_f32_e32 v20, 1.0, v28
	v_mul_f32_e32 v28, 0xc01d265f, v21
	v_rcp_f32_e32 v20, v20
	v_exp_f32_e32 v28, v28
	v_mul_f32_e32 v20, v27, v20
	v_add_f32_e32 v27, 1.0, v28
	v_rcp_f32_e32 v27, v27
	v_mul_f32_e32 v28, v29, v20
	v_fmamk_f32 v20, v68, 0x3d000000, v9
	v_med3_f32 v20, v20, s73, v210
	v_mul_f32_e32 v21, v21, v27
	v_fmamk_f32 v27, v73, 0x3d000000, v4
	v_min_f32_e32 v27, 0x40e00000, v27
	v_mul_f32_e32 v29, 0xc01d265f, v27
	v_exp_f32_e32 v29, v29
	v_mul_f32_e32 v30, v20, v21
	v_fmamk_f32 v20, v69, 0x3d000000, v3
	v_med3_f32 v31, v20, s73, v210
	v_add_f32_e32 v20, 1.0, v29
	v_rcp_f32_e32 v29, v20
	v_mov_b32_e32 v21, v169
	v_cvt_pk_fp8_f32 v21, v25, v28
	v_mov_b32_e32 v20, v169
	v_cvt_pk_fp8_f32 v20, v5, v23
	v_mul_f32_e32 v5, v27, v29
	v_mul_f32_e32 v5, v31, v5
	v_cvt_pk_fp8_f32 v21, v30, v5 op_sel:[0,0,1]
	v_fmamk_f32 v5, v62, 0x3d000000, v14
	v_min_f32_e32 v5, 0x40e00000, v5
	v_cvt_pk_fp8_f32 v20, v26, v22 op_sel:[0,0,1]
	v_mul_f32_e32 v22, 0xc01d265f, v5
	v_exp_f32_e32 v25, v22
	v_add_co_u32_e32 v22, vcc, s75, v18
	v_fmamk_f32 v29, v51, 0x3d000000, v7
	s_nop 0
	v_addc_co_u32_e32 v23, vcc, 0, v19, vcc
	global_store_dwordx2 v[22:23], v[20:21], off
	v_add_f32_e32 v21, 1.0, v25
	v_fmamk_f32 v22, v63, 0x3d000000, v16
	v_rcp_f32_e32 v21, v21
	v_min_f32_e32 v22, 0x40e00000, v22
	v_mul_f32_e32 v23, 0xc01d265f, v22
	v_exp_f32_e32 v23, v23
	v_fmamk_f32 v20, v58, 0x3d000000, v24
	v_mul_f32_e32 v5, v5, v21
	v_fmamk_f32 v21, v64, 0x3d000000, v10
	v_med3_f32 v20, v20, s73, v210
	v_min_f32_e32 v21, 0x40e00000, v21
	v_mul_f32_e32 v5, v20, v5
	v_add_f32_e32 v20, 1.0, v23
	v_mul_f32_e32 v23, 0xc01d265f, v21
	v_rcp_f32_e32 v20, v20
	v_exp_f32_e32 v23, v23
	v_fmamk_f32 v25, v59, 0x3d000000, v15
	v_med3_f32 v25, v25, s73, v210
	v_mul_f32_e32 v20, v22, v20
	v_add_f32_e32 v22, 1.0, v23
	v_rcp_f32_e32 v22, v22
	v_mul_f32_e32 v23, v25, v20
	v_fmamk_f32 v20, v60, 0x3d000000, v17
	v_med3_f32 v20, v20, s73, v210
	v_mul_f32_e32 v21, v21, v22
	v_fmamk_f32 v22, v65, 0x3d000000, v12
	v_min_f32_e32 v22, 0x40e00000, v22
	v_mul_f32_e32 v25, 0xc01d265f, v22
	v_exp_f32_e32 v25, v25
	v_mul_f32_e32 v26, v20, v21
	v_fmamk_f32 v20, v61, 0x3d000000, v13
	v_med3_f32 v20, v20, s73, v210
	v_add_f32_e32 v21, 1.0, v25
	v_fmamk_f32 v25, v54, 0x3d000000, v6
	v_min_f32_e32 v25, 0x40e00000, v25
	v_rcp_f32_e32 v21, v21
	v_mul_f32_e32 v27, 0xc01d265f, v25
	v_exp_f32_e32 v27, v27
	v_med3_f32 v29, v29, s73, v210
	v_mul_f32_e32 v21, v22, v21
	v_mul_f32_e32 v22, v20, v21
	v_add_f32_e32 v21, 1.0, v27
	v_rcp_f32_e32 v21, v21
	v_fmamk_f32 v27, v55, 0x3d000000, v8
	v_min_f32_e32 v27, 0x40e00000, v27
	v_mul_f32_e32 v28, 0xc01d265f, v27
	v_fmamk_f32 v20, v50, 0x3d000000, v11
	v_exp_f32_e32 v28, v28
	v_med3_f32 v20, v20, s73, v210
	v_mul_f32_e32 v21, v25, v21
	v_mul_f32_e32 v25, v20, v21
	v_fmamk_f32 v21, v56, 0x3d000000, v2
	v_min_f32_e32 v21, 0x40e00000, v21
	v_add_f32_e32 v20, 1.0, v28
	v_mul_f32_e32 v28, 0xc01d265f, v21
	v_rcp_f32_e32 v20, v20
	v_exp_f32_e32 v28, v28
	v_fmac_f32_e32 v16, 0x3d000000, v47
	v_min_f32_e32 v16, 0x40e00000, v16
	v_mul_f32_e32 v20, v27, v20
	v_add_f32_e32 v27, 1.0, v28
	v_rcp_f32_e32 v27, v27
	v_mul_f32_e32 v28, v29, v20
	v_fmamk_f32 v20, v52, 0x3d000000, v9
	v_med3_f32 v20, v20, s73, v210
	v_mul_f32_e32 v21, v21, v27
	v_fmamk_f32 v27, v57, 0x3d000000, v4
	v_min_f32_e32 v27, 0x40e00000, v27
	v_mul_f32_e32 v29, 0xc01d265f, v27
	v_exp_f32_e32 v29, v29
	v_mul_f32_e32 v30, v20, v21
	v_fmamk_f32 v20, v53, 0x3d000000, v3
	v_med3_f32 v31, v20, s73, v210
	v_add_f32_e32 v20, 1.0, v29
	v_rcp_f32_e32 v29, v20
	v_mov_b32_e32 v21, v169
	v_cvt_pk_fp8_f32 v21, v25, v28
	v_mov_b32_e32 v20, v169
	v_cvt_pk_fp8_f32 v20, v5, v23
	v_mul_f32_e32 v5, v27, v29
	v_mul_f32_e32 v5, v31, v5
	v_cvt_pk_fp8_f32 v21, v30, v5 op_sel:[0,0,1]
	v_fmamk_f32 v5, v46, 0x3d000000, v14
	v_min_f32_e32 v5, 0x40e00000, v5
	v_mul_f32_e32 v14, 0xc01d265f, v5
	v_cvt_pk_fp8_f32 v20, v26, v22 op_sel:[0,0,1]
	v_exp_f32_e32 v14, v14
	v_add_co_u32_e32 v22, vcc, s76, v18
	v_fmamk_f32 v10, v48, 0x3d000000, v10
	s_nop 0
	v_addc_co_u32_e32 v23, vcc, 0, v19, vcc
	global_store_dwordx2 v[22:23], v[20:21], off
	v_add_f32_e32 v14, 1.0, v14
	v_mul_f32_e32 v20, 0xc01d265f, v16
	v_rcp_f32_e32 v14, v14
	v_exp_f32_e32 v20, v20
	v_min_f32_e32 v10, 0x40e00000, v10
	v_fmac_f32_e32 v12, 0x3d000000, v49
	v_mul_f32_e32 v5, v5, v14
	v_add_f32_e32 v14, 1.0, v20
	v_mul_f32_e32 v20, 0xc01d265f, v10
	v_rcp_f32_e32 v14, v14
	v_exp_f32_e32 v20, v20
	v_min_f32_e32 v12, 0x40e00000, v12
	v_fmac_f32_e32 v15, 0x3d000000, v43
	v_mul_f32_e32 v14, v16, v14
	v_add_f32_e32 v16, 1.0, v20
	v_rcp_f32_e32 v16, v16
	v_med3_f32 v15, v15, s73, v210
	v_fmac_f32_e32 v17, 0x3d000000, v44
	v_mul_f32_e32 v14, v15, v14
	v_mul_f32_e32 v10, v10, v16
	v_mul_f32_e32 v16, 0xc01d265f, v12
	v_exp_f32_e32 v16, v16
	v_med3_f32 v15, v17, s73, v210
	v_fmamk_f32 v6, v38, 0x3d000000, v6
	v_mul_f32_e32 v10, v15, v10
	v_add_f32_e32 v15, 1.0, v16
	v_min_f32_e32 v6, 0x40e00000, v6
	v_rcp_f32_e32 v15, v15
	v_mul_f32_e32 v16, 0xc01d265f, v6
	v_exp_f32_e32 v16, v16
	v_fmac_f32_e32 v13, 0x3d000000, v45
	v_med3_f32 v13, v13, s73, v210
	v_mul_f32_e32 v12, v12, v15
	v_fmac_f32_e32 v8, 0x3d000000, v39
	v_mul_f32_e32 v12, v13, v12
	v_add_f32_e32 v13, 1.0, v16
	v_min_f32_e32 v8, 0x40e00000, v8
	v_rcp_f32_e32 v13, v13
	v_mul_f32_e32 v15, 0xc01d265f, v8
	v_exp_f32_e32 v15, v15
	v_fmac_f32_e32 v11, 0x3d000000, v34
	v_fmamk_f32 v2, v40, 0x3d000000, v2
	v_med3_f32 v11, v11, s73, v210
	v_mul_f32_e32 v6, v6, v13
	v_min_f32_e32 v2, 0x40e00000, v2
	v_mul_f32_e32 v6, v11, v6
	v_add_f32_e32 v11, 1.0, v15
	v_mul_f32_e32 v13, 0xc01d265f, v2
	v_rcp_f32_e32 v11, v11
	v_exp_f32_e32 v13, v13
	v_fmac_f32_e32 v7, 0x3d000000, v35
	v_fmac_f32_e32 v4, 0x3d000000, v41
	v_med3_f32 v7, v7, s73, v210
	v_mul_f32_e32 v8, v8, v11
	v_add_f32_e32 v11, 1.0, v13
	v_fmac_f32_e32 v9, 0x3d000000, v36
	v_min_f32_e32 v4, 0x40e00000, v4
	v_rcp_f32_e32 v11, v11
	v_mul_f32_e32 v7, v7, v8
	v_med3_f32 v8, v9, s73, v210
	v_mul_f32_e32 v9, 0xc01d265f, v4
	v_exp_f32_e32 v9, v9
	v_mul_f32_e32 v2, v2, v11
	v_fmac_f32_e32 v24, 0x3d000000, v42
	v_mul_f32_e32 v8, v8, v2
	v_add_f32_e32 v2, 1.0, v9
	v_med3_f32 v21, v24, s73, v210
	v_fmac_f32_e32 v3, 0x3d000000, v37
	v_rcp_f32_e32 v9, v2
	v_mul_f32_e32 v5, v21, v5
	v_med3_f32 v11, v3, s73, v210
	v_mov_b32_e32 v2, v169
	v_mov_b32_e32 v3, v169
	v_cvt_pk_fp8_f32 v2, v5, v14
	v_cvt_pk_fp8_f32 v3, v6, v7
	v_mul_f32_e32 v4, v4, v9
	v_mul_f32_e32 v4, v11, v4
	v_cvt_pk_fp8_f32 v2, v10, v12 op_sel:[0,0,1]
	v_cvt_pk_fp8_f32 v3, v8, v4 op_sel:[0,0,1]
	v_add_co_u32_e32 v4, vcc, 0x58000, v18
	s_nop 1
	v_addc_co_u32_e32 v5, vcc, 0, v19, vcc
	s_and_b64 vcc, exec, s[4:5]
	s_mov_b64 s[4:5], -1
	global_store_dwordx2 v[4:5], v[2:3], off
	s_cmp_eq_u32 s32, 0
	s_cbranch_scc1 .Lp7c_skip3
	s_waitcnt vmcnt(8)
	v_pk_mul_f32 v[216:217], v[216:217], v[252:253]
	v_pk_mul_f32 v[218:219], v[218:219], v[252:253]
	v_pk_mul_f32 v[220:221], v[220:221], v[252:253]
	v_pk_mul_f32 v[222:223], v[222:223], v[252:253]
	v_pk_mul_f32 v[224:225], v[224:225], v[252:253]
	v_pk_mul_f32 v[226:227], v[226:227], v[252:253]
	v_pk_mul_f32 v[228:229], v[228:229], v[252:253]
	v_pk_mul_f32 v[230:231], v[230:231], v[252:253]
	v_pk_mul_f32 v[232:233], v[232:233], v[252:253]
	v_pk_mul_f32 v[234:235], v[234:235], v[252:253]
	v_pk_mul_f32 v[236:237], v[236:237], v[252:253]
	v_pk_mul_f32 v[238:239], v[238:239], v[252:253]
	v_pk_mul_f32 v[240:241], v[240:241], v[252:253]
	v_pk_mul_f32 v[242:243], v[242:243], v[252:253]
	v_pk_mul_f32 v[244:245], v[244:245], v[252:253]
	v_pk_mul_f32 v[246:247], v[246:247], v[252:253]
	v_pk_mul_f32 v[130:131], v[130:131], v[252:253]
	v_pk_mul_f32 v[132:133], v[132:133], v[252:253]
	v_pk_mul_f32 v[134:135], v[134:135], v[252:253]
	v_pk_mul_f32 v[136:137], v[136:137], v[252:253]
	v_pk_mul_f32 v[138:139], v[138:139], v[252:253]
	v_pk_mul_f32 v[140:141], v[140:141], v[252:253]
	v_pk_mul_f32 v[142:143], v[142:143], v[252:253]
	v_pk_mul_f32 v[144:145], v[144:145], v[252:253]
	v_pk_mul_f32 v[146:147], v[146:147], v[252:253]
	v_pk_mul_f32 v[148:149], v[148:149], v[252:253]
	v_pk_mul_f32 v[150:151], v[150:151], v[252:253]
	v_pk_mul_f32 v[152:153], v[152:153], v[252:253]
	v_pk_mul_f32 v[154:155], v[154:155], v[252:253]
	v_pk_mul_f32 v[156:157], v[156:157], v[252:253]
	v_pk_mul_f32 v[158:159], v[158:159], v[252:253]
	v_pk_mul_f32 v[160:161], v[160:161], v[252:253]
	v_cvt_pk_fp8_f32 v34, v216, v220
	v_cvt_pk_fp8_f32 v35, v232, v236
	v_cvt_pk_fp8_f32 v36, v130, v134
	v_cvt_pk_fp8_f32 v37, v146, v150
	v_cvt_pk_fp8_f32 v34, v224, v228 op_sel:[0,0,1]
	v_cvt_pk_fp8_f32 v35, v240, v244 op_sel:[0,0,1]
	v_cvt_pk_fp8_f32 v36, v138, v142 op_sel:[0,0,1]
	v_cvt_pk_fp8_f32 v37, v154, v158 op_sel:[0,0,1]
	v_cvt_pk_fp8_f32 v38, v217, v221
	v_cvt_pk_fp8_f32 v39, v233, v237
	v_cvt_pk_fp8_f32 v40, v131, v135
	v_cvt_pk_fp8_f32 v41, v147, v151
	v_cvt_pk_fp8_f32 v38, v225, v229 op_sel:[0,0,1]
	v_cvt_pk_fp8_f32 v39, v241, v245 op_sel:[0,0,1]
	v_cvt_pk_fp8_f32 v40, v139, v143 op_sel:[0,0,1]
	v_cvt_pk_fp8_f32 v41, v155, v159 op_sel:[0,0,1]
	v_cvt_pk_fp8_f32 v42, v218, v222
	v_cvt_pk_fp8_f32 v43, v234, v238
	v_cvt_pk_fp8_f32 v44, v132, v136
	v_cvt_pk_fp8_f32 v45, v148, v152
	v_cvt_pk_fp8_f32 v42, v226, v230 op_sel:[0,0,1]
	v_cvt_pk_fp8_f32 v43, v242, v246 op_sel:[0,0,1]
	v_cvt_pk_fp8_f32 v44, v140, v144 op_sel:[0,0,1]
	v_cvt_pk_fp8_f32 v45, v156, v160 op_sel:[0,0,1]
	v_cvt_pk_fp8_f32 v46, v219, v223
	v_cvt_pk_fp8_f32 v47, v235, v239
	v_cvt_pk_fp8_f32 v48, v133, v137
	v_cvt_pk_fp8_f32 v49, v149, v153
	v_cvt_pk_fp8_f32 v46, v227, v231 op_sel:[0,0,1]
	v_cvt_pk_fp8_f32 v47, v243, v247 op_sel:[0,0,1]
	v_cvt_pk_fp8_f32 v48, v141, v145 op_sel:[0,0,1]
	v_cvt_pk_fp8_f32 v49, v157, v161 op_sel:[0,0,1]
	s_nop 1
	ds_bpermute_b32 v50, v248, v34
	ds_bpermute_b32 v51, v248, v35
	ds_bpermute_b32 v52, v248, v36
	ds_bpermute_b32 v53, v248, v37
	ds_bpermute_b32 v54, v248, v38
	ds_bpermute_b32 v55, v248, v39
	ds_bpermute_b32 v56, v248, v40
	ds_bpermute_b32 v57, v248, v41
	ds_bpermute_b32 v58, v248, v42
	ds_bpermute_b32 v59, v248, v43
	ds_bpermute_b32 v60, v248, v44
	ds_bpermute_b32 v61, v248, v45
	ds_bpermute_b32 v62, v248, v46
	ds_bpermute_b32 v63, v248, v47
	ds_bpermute_b32 v64, v248, v48
	ds_bpermute_b32 v65, v248, v49
	s_waitcnt lgkmcnt(0)
	global_store_dwordx4 v250, v[50:53], s[88:89] nt
	s_add_u32 s96, s88, 0x800
	s_addc_u32 s97, s89, 0
	global_store_dwordx4 v250, v[54:57], s[96:97] nt
	s_add_u32 s96, s88, 0x1000
	s_addc_u32 s97, s89, 0
	global_store_dwordx4 v250, v[58:61], s[96:97] nt
	s_add_u32 s96, s88, 0x1800
	s_addc_u32 s97, s89, 0
	global_store_dwordx4 v250, v[62:65], s[96:97] nt
.Lp7c_skip3:
	s_cbranch_vccnz .LBB0_717
	s_andn2_b64 vcc, exec, s[20:21]
	s_cbranch_vccnz .LBB0_716
	s_barrier
	s_branch .LBB0_716

.LBB0_734:
	s_add_u32 s10, s48, 0xc000
	v_lshrrev_b32_e32 v8, 6, v0
	v_and_b32_e32 v2, 0xfc, v1
	s_addc_u32 s11, s49, 0
	v_mul_u32_u24_e32 v1, 0x410, v8
	v_lshlrev_b32_e32 v4, 2, v2
	s_mov_b32 s4, 0x10400
	v_lshrrev_b32_e32 v39, 1, v0
	v_and_b32_e32 v5, 1, v0
	s_add_u32 s22, s16, 0x5ee00000
	v_add3_u32 v1, 0, v1, v4
	v_lshlrev_b32_e32 v4, 6, v5
	v_mad_u32_u24 v5, v5, s4, 0
	v_lshlrev_b32_e32 v7, 2, v39
	v_lshrrev_b32_e32 v6, 2, v0
	s_addc_u32 s23, s17, 0
	v_mov_b32_e32 v3, 0
	v_add3_u32 v40, v5, v4, v7
	v_lshlrev_b32_e32 v7, 7, v39
	s_movk_i32 s4, 0xff
	s_add_i32 s24, 0, 0x27fd0
	s_mov_b32 s5, 0
	v_cmp_eq_u32_e64 s[2:3], 0, v0
	v_or_b32_e32 v9, 8, v8
	v_add_u32_e32 v10, 0x2080, v1
	v_or_b32_e32 v11, 16, v8
	v_add_u32_e32 v12, 0x4100, v1
	v_or_b32_e32 v13, 24, v8
	v_add_u32_e32 v14, 0x6180, v1
	v_or_b32_e32 v15, 32, v8
	v_add_u32_e32 v16, 0x8200, v1
	v_or_b32_e32 v17, 40, v8
	v_add_u32_e32 v18, 0xa280, v1
	v_or_b32_e32 v19, 48, v8
	v_add_u32_e32 v20, 0xc300, v1
	v_or_b32_e32 v21, 56, v8
	v_add_u32_e32 v22, 0xe380, v1
	v_or_b32_e32 v23, 64, v8
	v_add_u32_e32 v24, 0x10400, v1
	v_or_b32_e32 v25, 0x48, v8
	v_add_u32_e32 v26, 0x12480, v1
	v_or_b32_e32 v27, 0x50, v8
	v_add_u32_e32 v28, 0x14500, v1
	v_or_b32_e32 v29, 0x58, v8
	v_add_u32_e32 v30, 0x16580, v1
	v_or_b32_e32 v31, 0x60, v8
	v_add_u32_e32 v32, 0x18600, v1
	v_or_b32_e32 v33, 0x68, v8
	v_add_u32_e32 v34, 0x1a680, v1
	v_or_b32_e32 v35, 0x70, v8
	v_add_u32_e32 v36, 0x1c700, v1
	v_or_b32_e32 v37, 0x78, v8
	v_add_u32_e32 v38, 0x1e7c0, v1
	v_mov_b32_e32 v5, v3
	v_bitop3_b32 v41, v7, s4, v6 bitop3:0xc8
	v_mov_b32_e32 v42, s24
	s_movk_i32 s25, 0xffff
	v_lshlrev_b32_e32 v2, 2, v2
	s_branch .LBB0_737

.LBB0_741:
	s_or_b64 exec, exec, s[16:17]
	s_waitcnt lgkmcnt(0)
	s_barrier
	ds_read_b32 v6, v42
	s_mov_b64 s[16:17], -1
	s_waitcnt lgkmcnt(0)
	v_cmp_lt_i32_e32 vcc, s25, v6
	v_readfirstlane_b32 s4, v6
	s_cbranch_vccnz .LBB0_736
	s_add_i32 s18, s4, 0x2380
	s_cmpk_gt_i32 s4, 0xfc7f
	s_cbranch_scc0 .LBB0_744
	s_addk_i32 s4, 0x380
	s_lshr_b32 s4, s4, 7
	s_lshl_b64 s[16:17], s[4:5], 22
	s_lshl_b64 s[20:21], s[4:5], 24
	s_add_u32 s19, s14, s20
	s_addc_u32 s21, s15, s21
	s_add_u32 s16, s22, s16
	s_addc_u32 s17, s23, s17
	s_lshl_b32 s20, s18, 8
	s_lshl_b32 s4, s18, 4
	s_and_b32 s27, s20, 0x700
	s_and_b32 s26, s4, 0x7f0
	s_and_b32 s4, s4, 0x780
	s_lshl_b32 s20, s27, 2
	s_add_u32 s20, s19, s20
	s_addc_u32 s21, s21, 0
	v_or_b32_e32 v43, s4, v8
	v_lshl_add_u64 v[6:7], s[20:21], 0, v[2:3]
	v_lshlrev_b32_e32 v44, 13, v43
	v_mov_b32_e32 v45, v3
	v_or_b32_e32 v43, s4, v9
	v_lshl_add_u64 v[52:53], v[6:7], 0, v[44:45]
	v_lshlrev_b32_e32 v44, 13, v43
	v_or_b32_e32 v43, s4, v11
	v_lshl_add_u64 v[54:55], v[6:7], 0, v[44:45]
	global_load_dwordx4 v[44:47], v[52:53], off
	global_load_dwordx4 v[48:51], v[54:55], off
	v_lshlrev_b32_e32 v52, 13, v43
	v_mov_b32_e32 v53, v3
	v_or_b32_e32 v43, s4, v13
	v_lshl_add_u64 v[60:61], v[6:7], 0, v[52:53]
	v_lshlrev_b32_e32 v52, 13, v43
	v_or_b32_e32 v43, s4, v15
	v_lshl_add_u64 v[62:63], v[6:7], 0, v[52:53]
	global_load_dwordx4 v[52:55], v[60:61], off
	global_load_dwordx4 v[56:59], v[62:63], off
	v_lshlrev_b32_e32 v60, 13, v43
	v_mov_b32_e32 v61, v3
	v_or_b32_e32 v43, s4, v17
	v_lshl_add_u64 v[68:69], v[6:7], 0, v[60:61]
	v_lshlrev_b32_e32 v60, 13, v43
	v_or_b32_e32 v43, s4, v19
	v_lshl_add_u64 v[70:71], v[6:7], 0, v[60:61]
	global_load_dwordx4 v[60:63], v[68:69], off
	global_load_dwordx4 v[64:67], v[70:71], off
	v_lshlrev_b32_e32 v68, 13, v43
	v_mov_b32_e32 v69, v3
	v_or_b32_e32 v43, s4, v21
	v_lshl_add_u64 v[76:77], v[6:7], 0, v[68:69]
	v_lshlrev_b32_e32 v68, 13, v43
	v_or_b32_e32 v43, s4, v23
	v_lshl_add_u64 v[78:79], v[6:7], 0, v[68:69]
	global_load_dwordx4 v[68:71], v[76:77], off
	global_load_dwordx4 v[72:75], v[78:79], off
	v_lshlrev_b32_e32 v76, 13, v43
	v_mov_b32_e32 v77, v3
	v_or_b32_e32 v43, s4, v25
	v_lshl_add_u64 v[84:85], v[6:7], 0, v[76:77]
	v_lshlrev_b32_e32 v76, 13, v43
	v_or_b32_e32 v43, s4, v27
	v_lshl_add_u64 v[86:87], v[6:7], 0, v[76:77]
	global_load_dwordx4 v[76:79], v[84:85], off
	global_load_dwordx4 v[80:83], v[86:87], off
	v_lshlrev_b32_e32 v84, 13, v43
	v_mov_b32_e32 v85, v3
	v_or_b32_e32 v43, s4, v29
	v_lshl_add_u64 v[92:93], v[6:7], 0, v[84:85]
	v_lshlrev_b32_e32 v84, 13, v43
	v_or_b32_e32 v43, s4, v31
	v_lshl_add_u64 v[94:95], v[6:7], 0, v[84:85]
	global_load_dwordx4 v[84:87], v[92:93], off
	global_load_dwordx4 v[88:91], v[94:95], off
	v_lshlrev_b32_e32 v92, 13, v43
	v_mov_b32_e32 v93, v3
	v_or_b32_e32 v43, s4, v33
	v_lshl_add_u64 v[100:101], v[6:7], 0, v[92:93]
	v_lshlrev_b32_e32 v92, 13, v43
	v_or_b32_e32 v43, s26, v35
	v_lshl_add_u64 v[102:103], v[6:7], 0, v[92:93]
	global_load_dwordx4 v[92:95], v[100:101], off
	global_load_dwordx4 v[96:99], v[102:103], off
	v_lshlrev_b32_e32 v100, 13, v43
	v_mov_b32_e32 v101, v3
	v_or_b32_e32 v43, s4, v37
	v_lshl_add_u64 v[108:109], v[6:7], 0, v[100:101]
	v_lshlrev_b32_e32 v100, 13, v43
	v_lshl_add_u64 v[6:7], v[6:7], 0, v[100:101]
	global_load_dwordx4 v[100:103], v[108:109], off
	global_load_dwordx4 v[104:107], v[6:7], off
	v_or_b32_e32 v6, s27, v39
	v_lshlrev_b32_e32 v6, 11, v6
	v_mov_b32_e32 v7, v3
	v_lshl_add_u64 v[6:7], s[16:17], 0, v[6:7]
	v_lshl_add_u64 v[6:7], v[6:7], 0, s[4:5]
	v_lshl_add_u64 v[6:7], v[6:7], 0, v[4:5]
	s_mov_b64 s[16:17], 0
	s_waitcnt vmcnt(15)
	ds_write_b128 v1, v[44:47]
	s_waitcnt vmcnt(14)
	ds_write_b128 v10, v[48:51]
	s_waitcnt vmcnt(13)
	ds_write_b128 v12, v[52:55]
	s_waitcnt vmcnt(12)
	ds_write_b128 v14, v[56:59]
	s_waitcnt vmcnt(11)
	ds_write_b128 v16, v[60:63]
	s_waitcnt vmcnt(10)
	ds_write_b128 v18, v[64:67]
	s_waitcnt vmcnt(9)
	ds_write_b128 v20, v[68:71]
	s_waitcnt vmcnt(8)
	ds_write_b128 v22, v[72:75]
	s_waitcnt vmcnt(7)
	ds_write_b128 v24, v[76:79] offset:64
	s_waitcnt vmcnt(6)
	ds_write_b128 v26, v[80:83] offset:64
	s_waitcnt vmcnt(5)
	ds_write_b128 v28, v[84:87] offset:64
	s_waitcnt vmcnt(4)
	ds_write_b128 v30, v[88:91] offset:64
	s_waitcnt vmcnt(3)
	ds_write_b128 v32, v[92:95] offset:64
	s_waitcnt vmcnt(2)
	ds_write_b128 v34, v[96:99] offset:64
	s_waitcnt vmcnt(1)
	ds_write_b128 v36, v[100:103] offset:64
	s_waitcnt vmcnt(0)
	ds_write_b128 v38, v[104:107]
	s_waitcnt lgkmcnt(0)
	s_barrier
	ds_read_b32 v43, v40
	ds_read_b32 v44, v40 offset:1040
	ds_read_b32 v45, v40 offset:2080
	ds_read_b32 v46, v40 offset:3120
	ds_read_b32 v47, v40 offset:4160
	ds_read_b32 v48, v40 offset:5200
	ds_read_b32 v49, v40 offset:6240
	ds_read_b32 v50, v40 offset:7280
	s_waitcnt lgkmcnt(6)
	v_mul_f32_e32 v51, 0x42000000, v44
	s_waitcnt lgkmcnt(5)
	v_mul_f32_e32 v52, 0x42000000, v45
	s_waitcnt lgkmcnt(4)
	v_mul_f32_e32 v53, 0x42000000, v46
	s_waitcnt lgkmcnt(3)
	v_mul_f32_e32 v46, 0x42000000, v47
	s_waitcnt lgkmcnt(2)
	v_mul_f32_e32 v47, 0x42000000, v48
	s_waitcnt lgkmcnt(1)
	v_mul_f32_e32 v48, 0x42000000, v49
	s_waitcnt lgkmcnt(0)
	v_mul_f32_e32 v49, 0x42000000, v50
	ds_read_b32 v44, v40 offset:8320
	ds_read_b32 v45, v40 offset:9360
	ds_read_b32 v50, v40 offset:10400
	ds_read_b32 v54, v40 offset:11440
	ds_read_b32 v55, v40 offset:12480
	ds_read_b32 v56, v40 offset:13520
	ds_read_b32 v57, v40 offset:14560
	ds_read_b32 v58, v40 offset:15600
	s_waitcnt lgkmcnt(6)
	v_mul_f32_e32 v60, 0x42000000, v45
	v_mov_b32_e32 v45, v3
	v_mul_f32_e32 v43, 0x42000000, v43
	v_mul_f32_e32 v59, 0x42000000, v44
	v_mov_b32_e32 v44, v3
	v_cvt_pk_fp8_f32 v45, v46, v47
	v_mov_b32_e32 v46, v3
	v_cvt_pk_fp8_f32 v44, v43, v51
	v_cvt_pk_fp8_f32 v46, v59, v60
	s_waitcnt lgkmcnt(5)
	v_mul_f32_e32 v50, 0x42000000, v50
	s_waitcnt lgkmcnt(4)
	v_mul_f32_e32 v54, 0x42000000, v54
	s_waitcnt lgkmcnt(3)
	v_mul_f32_e32 v55, 0x42000000, v55
	s_waitcnt lgkmcnt(2)
	v_mul_f32_e32 v56, 0x42000000, v56
	v_mov_b32_e32 v47, v3
	v_cvt_pk_fp8_f32 v44, v52, v53 op_sel:[0,0,1]
	v_cvt_pk_fp8_f32 v45, v48, v49 op_sel:[0,0,1]
	v_cvt_pk_fp8_f32 v46, v50, v54 op_sel:[0,0,1]
	ds_read_b32 v43, v40 offset:16640
	ds_read_b32 v48, v40 offset:17680
	ds_read_b32 v49, v40 offset:18720
	ds_read_b32 v50, v40 offset:19760
	ds_read_b32 v51, v40 offset:20800
	ds_read_b32 v52, v40 offset:21840
	ds_read_b32 v53, v40 offset:22880
	ds_read_b32 v54, v40 offset:23920
	v_cvt_pk_fp8_f32 v47, v55, v56
	s_waitcnt lgkmcnt(9)
	v_mul_f32_e32 v57, 0x42000000, v57
	s_waitcnt lgkmcnt(8)
	v_mul_f32_e32 v58, 0x42000000, v58
	s_waitcnt lgkmcnt(6)
	v_mul_f32_e32 v55, 0x42000000, v48
	v_cvt_pk_fp8_f32 v47, v57, v58 op_sel:[0,0,1]
	s_waitcnt lgkmcnt(5)
	v_mul_f32_e32 v56, 0x42000000, v49
	s_waitcnt lgkmcnt(4)
	v_mul_f32_e32 v57, 0x42000000, v50
	s_waitcnt lgkmcnt(3)
	v_mul_f32_e32 v50, 0x42000000, v51
	s_waitcnt lgkmcnt(2)
	v_mul_f32_e32 v51, 0x42000000, v52
	s_waitcnt lgkmcnt(1)
	v_mul_f32_e32 v52, 0x42000000, v53
	s_waitcnt lgkmcnt(0)
	v_mul_f32_e32 v53, 0x42000000, v54
	ds_read_b32 v48, v40 offset:24960
	ds_read_b32 v49, v40 offset:26000
	ds_read_b32 v54, v40 offset:27040
	ds_read_b32 v58, v40 offset:28080
	ds_read_b32 v59, v40 offset:29120
	ds_read_b32 v60, v40 offset:30160
	ds_read_b32 v61, v40 offset:31200
	ds_read_b32 v62, v40 offset:32240
	s_waitcnt lgkmcnt(6)
	v_mul_f32_e32 v64, 0x42000000, v49
	v_mov_b32_e32 v49, v3
	v_mul_f32_e32 v43, 0x42000000, v43
	v_mul_f32_e32 v63, 0x42000000, v48
	v_mov_b32_e32 v48, v3
	v_cvt_pk_fp8_f32 v49, v50, v51
	v_mov_b32_e32 v50, v3
	v_cvt_pk_fp8_f32 v48, v43, v55
	v_cvt_pk_fp8_f32 v50, v63, v64
	s_waitcnt lgkmcnt(5)
	v_mul_f32_e32 v54, 0x42000000, v54
	s_waitcnt lgkmcnt(4)
	v_mul_f32_e32 v58, 0x42000000, v58
	s_waitcnt lgkmcnt(3)
	v_mul_f32_e32 v59, 0x42000000, v59
	s_waitcnt lgkmcnt(2)
	v_mul_f32_e32 v60, 0x42000000, v60
	v_mov_b32_e32 v51, v3
	v_cvt_pk_fp8_f32 v48, v56, v57 op_sel:[0,0,1]
	v_cvt_pk_fp8_f32 v49, v52, v53 op_sel:[0,0,1]
	v_cvt_pk_fp8_f32 v50, v54, v58 op_sel:[0,0,1]
	ds_read_b32 v43, v40 offset:33280
	ds_read_b32 v52, v40 offset:34320
	ds_read_b32 v53, v40 offset:35360
	ds_read_b32 v54, v40 offset:36400
	ds_read_b32 v55, v40 offset:37440
	ds_read_b32 v56, v40 offset:38480
	ds_read_b32 v57, v40 offset:39520
	ds_read_b32 v58, v40 offset:40560
	v_cvt_pk_fp8_f32 v51, v59, v60
	s_waitcnt lgkmcnt(9)
	v_mul_f32_e32 v61, 0x42000000, v61
	s_waitcnt lgkmcnt(8)
	v_mul_f32_e32 v62, 0x42000000, v62
	s_waitcnt lgkmcnt(6)
	v_mul_f32_e32 v59, 0x42000000, v52
	v_cvt_pk_fp8_f32 v51, v61, v62 op_sel:[0,0,1]
	s_waitcnt lgkmcnt(5)
	v_mul_f32_e32 v60, 0x42000000, v53
	s_waitcnt lgkmcnt(4)
	v_mul_f32_e32 v61, 0x42000000, v54
	s_waitcnt lgkmcnt(3)
	v_mul_f32_e32 v54, 0x42000000, v55
	s_waitcnt lgkmcnt(2)
	v_mul_f32_e32 v55, 0x42000000, v56
	s_waitcnt lgkmcnt(1)
	v_mul_f32_e32 v56, 0x42000000, v57
	s_waitcnt lgkmcnt(0)
	v_mul_f32_e32 v57, 0x42000000, v58
	ds_read_b32 v52, v40 offset:41600
	ds_read_b32 v53, v40 offset:42640
	ds_read_b32 v58, v40 offset:43680
	ds_read_b32 v62, v40 offset:44720
	ds_read_b32 v63, v40 offset:45760
	ds_read_b32 v64, v40 offset:46800
	ds_read_b32 v65, v40 offset:47840
	ds_read_b32 v66, v40 offset:48880
	s_waitcnt lgkmcnt(6)
	v_mul_f32_e32 v68, 0x42000000, v53
	v_mov_b32_e32 v53, v3
	v_mul_f32_e32 v43, 0x42000000, v43
	v_mul_f32_e32 v67, 0x42000000, v52
	v_mov_b32_e32 v52, v3
	v_cvt_pk_fp8_f32 v53, v54, v55
	v_mov_b32_e32 v54, v3
	v_cvt_pk_fp8_f32 v52, v43, v59
	v_cvt_pk_fp8_f32 v54, v67, v68
	s_waitcnt lgkmcnt(5)
	v_mul_f32_e32 v58, 0x42000000, v58
	s_waitcnt lgkmcnt(4)
	v_mul_f32_e32 v62, 0x42000000, v62
	s_waitcnt lgkmcnt(3)
	v_mul_f32_e32 v63, 0x42000000, v63
	s_waitcnt lgkmcnt(2)
	v_mul_f32_e32 v64, 0x42000000, v64
	v_mov_b32_e32 v55, v3
	v_cvt_pk_fp8_f32 v52, v60, v61 op_sel:[0,0,1]
	v_cvt_pk_fp8_f32 v53, v56, v57 op_sel:[0,0,1]
	v_cvt_pk_fp8_f32 v54, v58, v62 op_sel:[0,0,1]
	ds_read_b32 v43, v40 offset:49920
	ds_read_b32 v56, v40 offset:50960
	ds_read_b32 v57, v40 offset:52000
	ds_read_b32 v58, v40 offset:53040
	ds_read_b32 v59, v40 offset:54080
	ds_read_b32 v60, v40 offset:55120
	ds_read_b32 v61, v40 offset:56160
	ds_read_b32 v62, v40 offset:57200
	v_cvt_pk_fp8_f32 v55, v63, v64
	s_waitcnt lgkmcnt(9)
	v_mul_f32_e32 v65, 0x42000000, v65
	s_waitcnt lgkmcnt(8)
	v_mul_f32_e32 v66, 0x42000000, v66
	s_waitcnt lgkmcnt(6)
	v_mul_f32_e32 v63, 0x42000000, v56
	v_cvt_pk_fp8_f32 v55, v65, v66 op_sel:[0,0,1]
	s_waitcnt lgkmcnt(5)
	v_mul_f32_e32 v64, 0x42000000, v57
	s_waitcnt lgkmcnt(4)
	v_mul_f32_e32 v65, 0x42000000, v58
	s_waitcnt lgkmcnt(3)
	v_mul_f32_e32 v58, 0x42000000, v59
	s_waitcnt lgkmcnt(2)
	v_mul_f32_e32 v59, 0x42000000, v60
	s_waitcnt lgkmcnt(1)
	v_mul_f32_e32 v60, 0x42000000, v61
	s_waitcnt lgkmcnt(0)
	v_mul_f32_e32 v61, 0x42000000, v62
	ds_read_b32 v56, v40 offset:58240
	ds_read_b32 v57, v40 offset:59280
	ds_read_b32 v62, v40 offset:60320
	ds_read_b32 v66, v40 offset:61360
	ds_read_b32 v67, v40 offset:62400
	ds_read_b32 v68, v40 offset:63440
	ds_read_b32 v69, v40 offset:64480
	ds_read_b32 v70, v40 offset:65520
	s_waitcnt lgkmcnt(6)
	v_mul_f32_e32 v72, 0x42000000, v57
	v_mov_b32_e32 v57, v3
	v_mul_f32_e32 v43, 0x42000000, v43
	v_mul_f32_e32 v71, 0x42000000, v56
	s_waitcnt lgkmcnt(3)
	v_mul_f32_e32 v67, 0x42000000, v67
	s_waitcnt lgkmcnt(2)
	v_mul_f32_e32 v68, 0x42000000, v68
	v_mov_b32_e32 v56, v3
	v_cvt_pk_fp8_f32 v57, v58, v59
	v_mov_b32_e32 v58, v3
	v_mov_b32_e32 v59, v3
	v_cvt_pk_fp8_f32 v56, v43, v63
	v_cvt_pk_fp8_f32 v58, v71, v72
	v_cvt_pk_fp8_f32 v59, v67, v68
	v_mul_f32_e32 v62, 0x42000000, v62
	v_mul_f32_e32 v66, 0x42000000, v66
	s_waitcnt lgkmcnt(1)
	v_mul_f32_e32 v69, 0x42000000, v69
	s_waitcnt lgkmcnt(0)
	v_mul_f32_e32 v70, 0x42000000, v70
	v_cvt_pk_fp8_f32 v56, v64, v65 op_sel:[0,0,1]
	v_cvt_pk_fp8_f32 v57, v60, v61 op_sel:[0,0,1]
	v_cvt_pk_fp8_f32 v58, v62, v66 op_sel:[0,0,1]
	v_cvt_pk_fp8_f32 v59, v69, v70 op_sel:[0,0,1]
	global_store_dwordx4 v[6:7], v[44:47], off
	global_store_dwordx4 v[6:7], v[48:51], off offset:16
	global_store_dwordx4 v[6:7], v[52:55], off offset:32
	global_store_dwordx4 v[6:7], v[56:59], off offset:48
	s_waitcnt lgkmcnt(0)
	s_barrier
